# router: expert slot counters bumped once per workgroup+expert (tokens parked in LDS, wave 0 ranks with ballots); mem-K/V row norms: 32 loads in flight
# speedup vs baseline: 1.0116x; 1.0116x over previous
.LBB0_925:
	v_add_co_u32_e32 v2, vcc, 0x1000, v2
	s_nop 1
	v_addc_co_u32_e32 v3, vcc, 0, v3, vcc
	global_load_dword v186, v[2:3], off offset:-4096
	global_load_dword v187, v[2:3], off offset:-3840
	global_load_dword v188, v[2:3], off offset:-3584
	global_load_dword v189, v[2:3], off offset:-3328
	global_load_dword v190, v[2:3], off offset:-3072
	global_load_dword v191, v[2:3], off offset:-2816
	global_load_dword v192, v[2:3], off offset:-2560
	global_load_dword v193, v[2:3], off offset:-2304
	global_load_dword v194, v[2:3], off offset:-2048
	global_load_dword v195, v[2:3], off offset:-1792
	global_load_dword v196, v[2:3], off offset:-1536
	global_load_dword v197, v[2:3], off offset:-1280
	global_load_dword v198, v[2:3], off offset:-1024
	global_load_dword v199, v[2:3], off offset:-768
	global_load_dword v200, v[2:3], off offset:-512
	global_load_dword v201, v[2:3], off offset:-256
	global_load_dword v202, v[2:3], off
	global_load_dword v203, v[2:3], off offset:256
	global_load_dword v204, v[2:3], off offset:512
	global_load_dword v205, v[2:3], off offset:768
	global_load_dword v206, v[2:3], off offset:1024
	global_load_dword v207, v[2:3], off offset:1280
	global_load_dword v208, v[2:3], off offset:1536
	global_load_dword v209, v[2:3], off offset:1792
	global_load_dword v210, v[2:3], off offset:2048
	global_load_dword v211, v[2:3], off offset:2304
	global_load_dword v212, v[2:3], off offset:2560
	global_load_dword v213, v[2:3], off offset:2816
	global_load_dword v214, v[2:3], off offset:3072
	global_load_dword v215, v[2:3], off offset:3328
	global_load_dword v216, v[2:3], off offset:3584
	global_load_dword v217, v[2:3], off offset:3840
	s_waitcnt vmcnt(31)
	v_fmac_f32_e32 v6, v186, v186
	s_waitcnt vmcnt(30)
	v_fmac_f32_e32 v6, v187, v187
	s_waitcnt vmcnt(29)
	v_fmac_f32_e32 v6, v188, v188
	s_waitcnt vmcnt(28)
	v_fmac_f32_e32 v6, v189, v189
	s_waitcnt vmcnt(27)
	v_fmac_f32_e32 v6, v190, v190
	s_waitcnt vmcnt(26)
	v_fmac_f32_e32 v6, v191, v191
	s_waitcnt vmcnt(25)
	v_fmac_f32_e32 v6, v192, v192
	s_waitcnt vmcnt(24)
	v_fmac_f32_e32 v6, v193, v193
	s_waitcnt vmcnt(23)
	v_fmac_f32_e32 v6, v194, v194
	s_waitcnt vmcnt(22)
	v_fmac_f32_e32 v6, v195, v195
	s_waitcnt vmcnt(21)
	v_fmac_f32_e32 v6, v196, v196
	s_waitcnt vmcnt(20)
	v_fmac_f32_e32 v6, v197, v197
	s_waitcnt vmcnt(19)
	v_fmac_f32_e32 v6, v198, v198
	s_waitcnt vmcnt(18)
	v_fmac_f32_e32 v6, v199, v199
	s_waitcnt vmcnt(17)
	v_fmac_f32_e32 v6, v200, v200
	s_waitcnt vmcnt(16)
	v_fmac_f32_e32 v6, v201, v201
	s_waitcnt vmcnt(15)
	v_fmac_f32_e32 v6, v202, v202
	s_waitcnt vmcnt(14)
	v_fmac_f32_e32 v6, v203, v203
	s_waitcnt vmcnt(13)
	v_fmac_f32_e32 v6, v204, v204
	s_waitcnt vmcnt(12)
	v_fmac_f32_e32 v6, v205, v205
	s_waitcnt vmcnt(11)
	v_fmac_f32_e32 v6, v206, v206
	s_waitcnt vmcnt(10)
	v_fmac_f32_e32 v6, v207, v207
	s_waitcnt vmcnt(9)
	v_fmac_f32_e32 v6, v208, v208
	s_waitcnt vmcnt(8)
	v_fmac_f32_e32 v6, v209, v209
	s_waitcnt vmcnt(7)
	v_fmac_f32_e32 v6, v210, v210
	s_waitcnt vmcnt(6)
	v_fmac_f32_e32 v6, v211, v211
	s_waitcnt vmcnt(5)
	v_fmac_f32_e32 v6, v212, v212
	s_waitcnt vmcnt(4)
	v_fmac_f32_e32 v6, v213, v213
	s_waitcnt vmcnt(3)
	v_fmac_f32_e32 v6, v214, v214
	s_waitcnt vmcnt(2)
	v_fmac_f32_e32 v6, v215, v215
	s_waitcnt vmcnt(1)
	v_fmac_f32_e32 v6, v216, v216
	s_waitcnt vmcnt(0)
	v_fmac_f32_e32 v6, v217, v217
	s_or_b64 exec, exec, s[2:3]
	v_mbcnt_lo_u32_b32 v2, -1, 0
	v_mbcnt_hi_u32_b32 v2, -1, v2
	v_mbcnt_lo_u32_b32 v3, -1, 0
	v_mbcnt_hi_u32_b32 v3, -1, v3
	v_cmp_eq_u32_e64 s[2:3], 0, v5
	v_lshlrev_b32_e32 v2, 2, v2
	v_xor_b32_e32 v2, 4, v2
	ds_bpermute_b32 v2, v2, v6
	v_lshlrev_b32_e32 v3, 2, v3
	v_xor_b32_e32 v3, 8, v3
	s_waitcnt lgkmcnt(0)
	v_add_f32_e32 v2, v6, v2
	ds_bpermute_b32 v3, v3, v2
	v_mbcnt_lo_u32_b32 v6, -1, 0
	v_mbcnt_hi_u32_b32 v6, -1, v6
	s_waitcnt lgkmcnt(0)
	v_add_f32_e32 v2, v2, v3
	v_lshlrev_b32_e32 v6, 2, v6
	v_xor_b32_e32 v6, 16, v6
	ds_bpermute_b32 v3, v6, v2
	v_mbcnt_lo_u32_b32 v6, -1, 0
	v_mbcnt_hi_u32_b32 v6, -1, v6
	s_waitcnt lgkmcnt(0)
	v_add_f32_e32 v2, v2, v3
	v_lshlrev_b32_e32 v6, 2, v6
	v_xor_b32_e32 v6, 32, v6
	ds_bpermute_b32 v3, v6, v2
	v_mbcnt_lo_u32_b32 v6, -1, 0
	v_mbcnt_hi_u32_b32 v6, -1, v6
	s_waitcnt lgkmcnt(0)
	v_add_f32_e32 v2, v2, v3
	v_lshlrev_b32_e32 v6, 2, v6
	v_xor_b32_e32 v6, 64, v6
	ds_bpermute_b32 v3, v6, v2
	v_mbcnt_lo_u32_b32 v6, -1, 0
	v_mbcnt_hi_u32_b32 v6, -1, v6
	s_waitcnt lgkmcnt(0)
	v_add_f32_e32 v2, v2, v3
	v_lshlrev_b32_e32 v6, 2, v6
	v_xor_b32_e32 v3, 0x80, v6
	ds_bpermute_b32 v3, v3, v2
	s_and_saveexec_b64 s[24:25], s[2:3]
	s_cbranch_execz .LBB0_928
	s_waitcnt lgkmcnt(0)
	v_add_f32_e32 v2, v2, v3
	v_fmamk_f32 v2, v2, 0x3a000000, v100
	v_mul_f32_e32 v3, 0x4f800000, v2
	v_cmp_gt_f32_e32 vcc, s51, v2
	s_nop 1
	v_cndmask_b32_e32 v2, v2, v3, vcc
	v_sqrt_f32_e32 v3, v2
	s_nop 0
	v_add_u32_e32 v5, -1, v3
	v_fma_f32 v7, -v5, v3, v2
	v_add_u32_e32 v6, 1, v3
	v_cmp_ge_f32_e64 s[4:5], 0, v7
	s_nop 1
	v_cndmask_b32_e64 v5, v3, v5, s[4:5]
	v_fma_f32 v3, -v6, v3, v2
	v_cmp_lt_f32_e64 s[4:5], 0, v3
	s_nop 1
	v_cndmask_b32_e64 v3, v5, v6, s[4:5]
	v_mul_f32_e32 v5, 0x37800000, v3
	v_cndmask_b32_e32 v3, v3, v5, vcc
	v_cmp_class_f32_e32 vcc, v2, v101
	s_nop 1
	v_cndmask_b32_e32 v2, v3, v2, vcc
	v_div_scale_f32 v3, s[4:5], v2, v2, 1.0
	v_rcp_f32_e32 v5, v3
	s_nop 0
	v_fma_f32 v6, -v3, v5, 1.0
	v_fmac_f32_e32 v5, v6, v5
	v_div_scale_f32 v6, vcc, 1.0, v2, 1.0
	v_mul_f32_e32 v7, v6, v5
	v_fma_f32 v8, -v3, v7, v6
	v_fmac_f32_e32 v7, v8, v5
	v_fma_f32 v3, -v3, v7, v6
	v_div_fmas_f32 v3, v3, v5, v7
	v_div_fixup_f32 v2, v3, v2, 1.0
	v_mov_b32_e32 v3, s39
	ds_write_b32 v3, v2

.LBB0_929:
	v_add_co_u32_e32 v2, vcc, 0x1000, v2
	s_nop 1
	v_addc_co_u32_e32 v3, vcc, 0, v3, vcc
	global_load_dword v186, v[2:3], off offset:-4096
	global_load_dword v187, v[2:3], off offset:-3840
	global_load_dword v188, v[2:3], off offset:-3584
	global_load_dword v189, v[2:3], off offset:-3328
	global_load_dword v190, v[2:3], off offset:-3072
	global_load_dword v191, v[2:3], off offset:-2816
	global_load_dword v192, v[2:3], off offset:-2560
	global_load_dword v193, v[2:3], off offset:-2304
	global_load_dword v194, v[2:3], off offset:-2048
	global_load_dword v195, v[2:3], off offset:-1792
	global_load_dword v196, v[2:3], off offset:-1536
	global_load_dword v197, v[2:3], off offset:-1280
	global_load_dword v198, v[2:3], off offset:-1024
	global_load_dword v199, v[2:3], off offset:-768
	global_load_dword v200, v[2:3], off offset:-512
	global_load_dword v201, v[2:3], off offset:-256
	global_load_dword v202, v[2:3], off
	global_load_dword v203, v[2:3], off offset:256
	global_load_dword v204, v[2:3], off offset:512
	global_load_dword v205, v[2:3], off offset:768
	global_load_dword v206, v[2:3], off offset:1024
	global_load_dword v207, v[2:3], off offset:1280
	global_load_dword v208, v[2:3], off offset:1536
	global_load_dword v209, v[2:3], off offset:1792
	global_load_dword v210, v[2:3], off offset:2048
	global_load_dword v211, v[2:3], off offset:2304
	global_load_dword v212, v[2:3], off offset:2560
	global_load_dword v213, v[2:3], off offset:2816
	global_load_dword v214, v[2:3], off offset:3072
	global_load_dword v215, v[2:3], off offset:3328
	global_load_dword v216, v[2:3], off offset:3584
	global_load_dword v217, v[2:3], off offset:3840
	s_waitcnt vmcnt(31)
	v_fmac_f32_e32 v0, v186, v186
	s_waitcnt vmcnt(30)
	v_fmac_f32_e32 v0, v187, v187
	s_waitcnt vmcnt(29)
	v_fmac_f32_e32 v0, v188, v188
	s_waitcnt vmcnt(28)
	v_fmac_f32_e32 v0, v189, v189
	s_waitcnt vmcnt(27)
	v_fmac_f32_e32 v0, v190, v190
	s_waitcnt vmcnt(26)
	v_fmac_f32_e32 v0, v191, v191
	s_waitcnt vmcnt(25)
	v_fmac_f32_e32 v0, v192, v192
	s_waitcnt vmcnt(24)
	v_fmac_f32_e32 v0, v193, v193
	s_waitcnt vmcnt(23)
	v_fmac_f32_e32 v0, v194, v194
	s_waitcnt vmcnt(22)
	v_fmac_f32_e32 v0, v195, v195
	s_waitcnt vmcnt(21)
	v_fmac_f32_e32 v0, v196, v196
	s_waitcnt vmcnt(20)
	v_fmac_f32_e32 v0, v197, v197
	s_waitcnt vmcnt(19)
	v_fmac_f32_e32 v0, v198, v198
	s_waitcnt vmcnt(18)
	v_fmac_f32_e32 v0, v199, v199
	s_waitcnt vmcnt(17)
	v_fmac_f32_e32 v0, v200, v200
	s_waitcnt vmcnt(16)
	v_fmac_f32_e32 v0, v201, v201
	s_waitcnt vmcnt(15)
	v_fmac_f32_e32 v0, v202, v202
	s_waitcnt vmcnt(14)
	v_fmac_f32_e32 v0, v203, v203
	s_waitcnt vmcnt(13)
	v_fmac_f32_e32 v0, v204, v204
	s_waitcnt vmcnt(12)
	v_fmac_f32_e32 v0, v205, v205
	s_waitcnt vmcnt(11)
	v_fmac_f32_e32 v0, v206, v206
	s_waitcnt vmcnt(10)
	v_fmac_f32_e32 v0, v207, v207
	s_waitcnt vmcnt(9)
	v_fmac_f32_e32 v0, v208, v208
	s_waitcnt vmcnt(8)
	v_fmac_f32_e32 v0, v209, v209
	s_waitcnt vmcnt(7)
	v_fmac_f32_e32 v0, v210, v210
	s_waitcnt vmcnt(6)
	v_fmac_f32_e32 v0, v211, v211
	s_waitcnt vmcnt(5)
	v_fmac_f32_e32 v0, v212, v212
	s_waitcnt vmcnt(4)
	v_fmac_f32_e32 v0, v213, v213
	s_waitcnt vmcnt(3)
	v_fmac_f32_e32 v0, v214, v214
	s_waitcnt vmcnt(2)
	v_fmac_f32_e32 v0, v215, v215
	s_waitcnt vmcnt(1)
	v_fmac_f32_e32 v0, v216, v216
	s_waitcnt vmcnt(0)
	v_fmac_f32_e32 v0, v217, v217
	s_or_b64 exec, exec, s[4:5]
	v_mbcnt_lo_u32_b32 v2, -1, 0
	v_mbcnt_hi_u32_b32 v2, -1, v2
	v_mbcnt_lo_u32_b32 v3, -1, 0
	v_mbcnt_hi_u32_b32 v3, -1, v3
	s_nop 0
	v_lshlrev_b32_e32 v2, 2, v2
	v_xor_b32_e32 v2, 4, v2
	ds_bpermute_b32 v2, v2, v0
	v_lshlrev_b32_e32 v3, 2, v3
	v_xor_b32_e32 v3, 8, v3
	s_waitcnt lgkmcnt(0)
	v_add_f32_e32 v0, v0, v2
	ds_bpermute_b32 v2, v3, v0
	v_mbcnt_lo_u32_b32 v3, -1, 0
	v_mbcnt_hi_u32_b32 v3, -1, v3
	s_waitcnt lgkmcnt(0)
	v_add_f32_e32 v0, v0, v2
	v_lshlrev_b32_e32 v3, 2, v3
	v_xor_b32_e32 v3, 16, v3
	ds_bpermute_b32 v2, v3, v0
	v_mbcnt_lo_u32_b32 v3, -1, 0
	v_mbcnt_hi_u32_b32 v3, -1, v3
	s_waitcnt lgkmcnt(0)
	v_add_f32_e32 v0, v0, v2
	v_lshlrev_b32_e32 v3, 2, v3
	v_xor_b32_e32 v3, 32, v3
	ds_bpermute_b32 v2, v3, v0
	v_mbcnt_lo_u32_b32 v3, -1, 0
	v_mbcnt_hi_u32_b32 v3, -1, v3
	s_waitcnt lgkmcnt(0)
	v_add_f32_e32 v0, v0, v2
	v_lshlrev_b32_e32 v3, 2, v3
	v_xor_b32_e32 v3, 64, v3
	ds_bpermute_b32 v2, v3, v0
	v_mbcnt_lo_u32_b32 v3, -1, 0
	v_mbcnt_hi_u32_b32 v3, -1, v3
	s_waitcnt lgkmcnt(0)
	v_add_f32_e32 v0, v0, v2
	v_lshlrev_b32_e32 v3, 2, v3
	v_xor_b32_e32 v2, 0x80, v3
	ds_bpermute_b32 v2, v2, v0
	s_and_saveexec_b64 s[24:25], s[2:3]
	s_cbranch_execz .LBB0_932
	s_waitcnt lgkmcnt(0)
	v_add_f32_e32 v0, v0, v2
	v_fmamk_f32 v0, v0, 0x3a000000, v100
	v_mul_f32_e32 v2, 0x4f800000, v0
	v_cmp_gt_f32_e32 vcc, s51, v0
	s_nop 1
	v_cndmask_b32_e32 v0, v0, v2, vcc
	v_sqrt_f32_e32 v2, v0
	s_nop 0
	v_add_u32_e32 v3, -1, v2
	v_fma_f32 v5, -v3, v2, v0
	v_add_u32_e32 v4, 1, v2
	v_cmp_ge_f32_e64 s[4:5], 0, v5
	s_nop 1
	v_cndmask_b32_e64 v3, v2, v3, s[4:5]
	v_fma_f32 v2, -v4, v2, v0
	v_cmp_lt_f32_e64 s[4:5], 0, v2
	s_nop 1
	v_cndmask_b32_e64 v2, v3, v4, s[4:5]
	v_mul_f32_e32 v3, 0x37800000, v2
	v_cndmask_b32_e32 v2, v2, v3, vcc
	v_cmp_class_f32_e32 vcc, v0, v101
	s_nop 1
	v_cndmask_b32_e32 v0, v2, v0, vcc
	v_div_scale_f32 v2, s[4:5], v0, v0, 1.0
	v_rcp_f32_e32 v3, v2
	s_nop 0
	v_fma_f32 v4, -v2, v3, 1.0
	v_fmac_f32_e32 v3, v4, v3
	v_div_scale_f32 v4, vcc, 1.0, v0, 1.0
	v_mul_f32_e32 v5, v4, v3
	v_fma_f32 v6, -v2, v5, v4
	v_fmac_f32_e32 v5, v6, v3
	v_fma_f32 v2, -v2, v5, v4
	v_div_fmas_f32 v2, v2, v3, v5
	v_div_fixup_f32 v0, v2, v0, 1.0
	v_mov_b32_e32 v2, s44
	ds_write_b32 v2, v0

.LBB0_1619:
	s_or_b64 exec, exec, s[0:1]
	s_mov_b64 exec, 0xff
	v_mbcnt_lo_u32_b32 v80, -1, 0
	v_mbcnt_hi_u32_b32 v80, -1, v80
	s_lshl_b32 s98, s91, 8
	s_add_i32 s98, s98, 0x10000
	v_lshl_add_u32 v80, v80, 5, s98
	v_mov_b32_e32 v81, 0xff
	ds_write_b32 v80, v81
	s_mov_b64 exec, -1
	s_lshl_b32 s0, s13, 3
	s_add_i32 s56, s0, s91
	s_cmpk_gt_i32 s56, 0x3fff
	s_waitcnt vmcnt(16) lgkmcnt(0)
	s_barrier
	s_cbranch_scc1 .LBB0_1624
	s_lshl_b32 s58, s12, 3
	s_add_u32 s68, s52, 0x300000
	s_addc_u32 s69, s53, 0
	s_add_u32 s70, s52, 0x380000
	s_addc_u32 s71, s53, 0
	s_add_u32 s2, s52, 0x420000
	s_addc_u32 s3, s53, 0
	s_add_u32 s4, s52, 0x440000
	s_addc_u32 s5, s53, 0
	s_ashr_i32 s57, s56, 31
	s_lshl_b64 s[0:1], s[56:57], 2
	s_add_u32 s8, s0, 0x400000
	v_and_b32_e32 v0, 63, v0
	s_addc_u32 s9, s1, 0
	s_lshl_b64 s[0:1], s[56:57], 12
	s_ashr_i32 s59, s58, 31
	v_lshl_or_b32 v18, v0, 3, s0
	v_mov_b32_e32 v19, s1
	s_lshl_b32 s0, s13, 4
	v_readlane_b32 s1, v254, 53
	v_cmp_eq_u32_e64 s[36:37], 0, v0
	v_lshl_add_u32 v25, v0, 4, 0
	s_lshl_b64 s[72:73], s[58:59], 2
	s_lshl_b64 s[76:77], s[58:59], 12
	s_add_i32 s66, s1, s0
	s_lshl_b32 s12, s12, 4
	s_lshl_b32 s99, s91, 8
	s_add_i32 s99, s99, 0x10000
	s_branch .LBB0_1622

.LBB0_1622:
	v_lshl_add_u64 v[0:1], s[52:53], 0, v[18:19]
	s_waitcnt lgkmcnt(0)
	v_add_co_u32_e32 v20, vcc, 0x2d000000, v0
	s_nop 1
	v_addc_co_u32_e32 v21, vcc, 0, v1, vcc
	global_load_dwordx2 v[60:61], v[20:21], off
	global_load_dwordx2 v[62:63], v[20:21], off offset:512
	global_load_dwordx2 v[64:65], v[20:21], off offset:1024
	global_load_dwordx2 v[66:67], v[20:21], off offset:1536
	global_load_dwordx2 v[68:69], v[20:21], off offset:2048
	global_load_dwordx2 v[70:71], v[20:21], off offset:2560
	global_load_dwordx2 v[72:73], v[20:21], off offset:3072
	global_load_dwordx2 v[74:75], v[20:21], off offset:3584
	s_waitcnt vmcnt(7)
	v_mov_b32_e32 v0, v60
	v_mov_b32_e32 v1, v61
	v_lshlrev_b32_e32 v26, 16, v0
	v_and_b32_e32 v28, 0xffff0000, v0
	v_lshlrev_b32_e32 v30, 16, v1
	v_and_b32_e32 v32, 0xffff0000, v1
	ds_read_b128 v[0:3], v25
	ds_read_b128 v[4:7], v25 offset:32768
	v_mul_f32_e32 v40, v28, v28
	v_fmac_f32_e32 v40, v26, v26
	v_fmac_f32_e32 v40, v30, v30
	s_waitcnt lgkmcnt(1)
	v_fma_f32 v39, v2, v26, 0
	v_fma_f32 v37, v3, v26, 0
	s_waitcnt lgkmcnt(0)
	v_fma_f32 v35, v4, v26, 0
	v_fma_f32 v33, v5, v26, 0
	v_fma_f32 v31, v6, v26, 0
	v_fma_f32 v29, v7, v26, 0
	ds_read_b128 v[2:5], v25 offset:8192
	ds_read_b128 v[6:9], v25 offset:40960
	v_pk_fma_f32 v[0:1], v[0:1], v[26:27], 0 op_sel_hi:[1,0,0]
	v_fmac_f32_e32 v40, v32, v32
	s_waitcnt lgkmcnt(1)
	v_fmac_f32_e32 v39, v4, v28
	v_fmac_f32_e32 v37, v5, v28
	s_waitcnt lgkmcnt(0)
	v_fmac_f32_e32 v35, v6, v28
	v_fmac_f32_e32 v33, v7, v28
	v_fmac_f32_e32 v31, v8, v28
	v_fmac_f32_e32 v29, v9, v28
	ds_read_b128 v[4:7], v25 offset:16384
	ds_read_b128 v[8:11], v25 offset:49152
	s_waitcnt lgkmcnt(1)
	v_fmac_f32_e32 v39, v6, v30
	v_fmac_f32_e32 v37, v7, v30
	s_waitcnt lgkmcnt(0)
	v_fmac_f32_e32 v35, v8, v30
	v_fmac_f32_e32 v33, v9, v30
	v_fmac_f32_e32 v31, v10, v30
	v_fmac_f32_e32 v29, v11, v30
	ds_read_b128 v[6:9], v25 offset:24576
	ds_read_b128 v[10:13], v25 offset:57344
	s_waitcnt lgkmcnt(1)
	v_fmac_f32_e32 v39, v8, v32
	v_fmac_f32_e32 v37, v9, v32
	s_waitcnt lgkmcnt(0)
	v_fmac_f32_e32 v35, v10, v32
	v_fmac_f32_e32 v33, v11, v32
	v_fmac_f32_e32 v31, v12, v32
	v_fmac_f32_e32 v29, v13, v32
	v_pk_fma_f32 v[0:1], v[2:3], v[28:29], v[0:1] op_sel_hi:[1,0,1]
	s_waitcnt vmcnt(6)
	v_mov_b32_e32 v8, v62
	v_mov_b32_e32 v9, v63
	v_lshlrev_b32_e32 v34, 16, v8
	v_and_b32_e32 v16, 0xffff0000, v8
	v_lshlrev_b32_e32 v22, 16, v9
	v_and_b32_e32 v24, 0xffff0000, v9
	ds_read_b128 v[8:11], v25 offset:1024
	ds_read_b128 v[12:15], v25 offset:33792
	v_pk_fma_f32 v[0:1], v[4:5], v[30:31], v[0:1] op_sel_hi:[1,0,1]
	v_fmac_f32_e32 v40, v34, v34
	v_pk_fma_f32 v[0:1], v[6:7], v[32:33], v[0:1] op_sel_hi:[1,0,1]
	s_waitcnt lgkmcnt(1)
	v_fmac_f32_e32 v39, v10, v34
	v_pk_fma_f32 v[26:27], v[8:9], v[34:35], v[0:1] op_sel_hi:[1,0,1]
	ds_read_b128 v[0:3], v25 offset:9216
	ds_read_b128 v[4:7], v25 offset:41984
	v_fmac_f32_e32 v37, v11, v34
	s_waitcnt lgkmcnt(2)
	v_fmac_f32_e32 v35, v12, v34
	v_fmac_f32_e32 v33, v13, v34
	v_fmac_f32_e32 v31, v14, v34
	v_fmac_f32_e32 v29, v15, v34
	s_waitcnt lgkmcnt(1)
	v_fmac_f32_e32 v39, v2, v16
	v_fmac_f32_e32 v37, v3, v16
	s_waitcnt lgkmcnt(0)
	v_fmac_f32_e32 v35, v4, v16
	v_fmac_f32_e32 v33, v5, v16
	v_fmac_f32_e32 v31, v6, v16
	v_fmac_f32_e32 v29, v7, v16
	ds_read_b128 v[2:5], v25 offset:17408
	ds_read_b128 v[6:9], v25 offset:50176
	v_pk_fma_f32 v[0:1], v[0:1], v[16:17], v[26:27] op_sel_hi:[1,0,1]
	v_fmac_f32_e32 v40, v16, v16
	v_fmac_f32_e32 v40, v22, v22
	s_waitcnt lgkmcnt(1)
	v_fmac_f32_e32 v39, v4, v22
	v_fmac_f32_e32 v37, v5, v22
	s_waitcnt lgkmcnt(0)
	v_fmac_f32_e32 v35, v6, v22
	v_fmac_f32_e32 v33, v7, v22
	v_fmac_f32_e32 v31, v8, v22
	v_fmac_f32_e32 v29, v9, v22
	ds_read_b128 v[4:7], v25 offset:25600
	ds_read_b128 v[8:11], v25 offset:58368
	v_pk_fma_f32 v[0:1], v[2:3], v[22:23], v[0:1] op_sel_hi:[1,0,1]
	v_fmac_f32_e32 v40, v24, v24
	s_waitcnt lgkmcnt(1)
	v_fmac_f32_e32 v39, v6, v24
	v_fmac_f32_e32 v37, v7, v24
	s_waitcnt lgkmcnt(0)
	v_fmac_f32_e32 v35, v8, v24
	v_fmac_f32_e32 v33, v9, v24
	v_fmac_f32_e32 v31, v10, v24
	v_fmac_f32_e32 v29, v11, v24
	v_pk_fma_f32 v[0:1], v[4:5], v[24:25], v[0:1] op_sel_hi:[1,0,1]
	s_waitcnt vmcnt(5)
	v_mov_b32_e32 v6, v64
	v_mov_b32_e32 v7, v65
	v_lshlrev_b32_e32 v28, 16, v6
	v_and_b32_e32 v30, 0xffff0000, v6
	v_lshlrev_b32_e32 v32, 16, v7
	v_and_b32_e32 v34, 0xffff0000, v7
	ds_read_b128 v[6:9], v25 offset:2048
	ds_read_b128 v[10:13], v25 offset:34816
	v_fmac_f32_e32 v40, v28, v28
	v_fmac_f32_e32 v40, v30, v30
	v_fmac_f32_e32 v40, v32, v32
	s_waitcnt lgkmcnt(1)
	v_fmac_f32_e32 v39, v8, v28
	v_fmac_f32_e32 v37, v9, v28
	s_waitcnt lgkmcnt(0)
	v_fmac_f32_e32 v35, v10, v28
	v_fmac_f32_e32 v33, v11, v28
	v_fmac_f32_e32 v31, v12, v28
	v_fmac_f32_e32 v29, v13, v28
	ds_read_b128 v[8:11], v25 offset:10240
	ds_read_b128 v[12:15], v25 offset:43008
	v_fmac_f32_e32 v40, v34, v34
	s_waitcnt lgkmcnt(1)
	v_fmac_f32_e32 v39, v10, v30
	v_fmac_f32_e32 v37, v11, v30
	s_waitcnt lgkmcnt(0)
	v_fmac_f32_e32 v35, v12, v30
	v_fmac_f32_e32 v33, v13, v30
	ds_read_b128 v[10:13], v25 offset:18432
	ds_read_b128 v[42:45], v25 offset:51200
	v_fmac_f32_e32 v31, v14, v30
	v_fmac_f32_e32 v29, v15, v30
	s_waitcnt lgkmcnt(1)
	v_fmac_f32_e32 v39, v12, v32
	v_fmac_f32_e32 v37, v13, v32
	s_waitcnt lgkmcnt(0)
	v_fmac_f32_e32 v35, v42, v32
	v_fmac_f32_e32 v33, v43, v32
	v_fmac_f32_e32 v31, v44, v32
	v_fmac_f32_e32 v29, v45, v32
	ds_read_b128 v[12:15], v25 offset:26624
	ds_read_b128 v[42:45], v25 offset:59392
	s_waitcnt lgkmcnt(1)
	v_fmac_f32_e32 v39, v14, v34
	v_fmac_f32_e32 v37, v15, v34
	s_waitcnt lgkmcnt(0)
	v_fmac_f32_e32 v35, v42, v34
	v_fmac_f32_e32 v33, v43, v34
	v_fmac_f32_e32 v31, v44, v34
	v_fmac_f32_e32 v29, v45, v34
	ds_read_b128 v[42:45], v25 offset:3072
	ds_read_b128 v[46:49], v25 offset:35840
	s_waitcnt vmcnt(4)
	v_mov_b32_e32 v14, v66
	v_mov_b32_e32 v15, v67
	v_lshlrev_b32_e32 v36, 16, v14
	s_waitcnt lgkmcnt(1)
	v_fmac_f32_e32 v39, v44, v36
	v_fmac_f32_e32 v37, v45, v36
	s_waitcnt lgkmcnt(0)
	v_fmac_f32_e32 v35, v46, v36
	v_fmac_f32_e32 v33, v47, v36
	v_fmac_f32_e32 v31, v48, v36
	v_fmac_f32_e32 v29, v49, v36
	ds_read_b128 v[44:47], v25 offset:11264
	ds_read_b128 v[48:51], v25 offset:44032
	v_and_b32_e32 v14, 0xffff0000, v14
	v_lshlrev_b32_e32 v38, 16, v15
	v_and_b32_e32 v56, 0xffff0000, v15
	s_waitcnt lgkmcnt(1)
	v_fmac_f32_e32 v39, v46, v14
	v_fmac_f32_e32 v37, v47, v14
	s_waitcnt lgkmcnt(0)
	v_fmac_f32_e32 v35, v48, v14
	v_fmac_f32_e32 v33, v49, v14
	v_fmac_f32_e32 v31, v50, v14
	v_fmac_f32_e32 v29, v51, v14
	ds_read_b128 v[46:49], v25 offset:19456
	ds_read_b128 v[50:53], v25 offset:52224
	v_fmac_f32_e32 v40, v36, v36
	v_fmac_f32_e32 v40, v14, v14
	v_fmac_f32_e32 v40, v38, v38
	s_waitcnt lgkmcnt(1)
	v_fmac_f32_e32 v39, v48, v38
	s_waitcnt lgkmcnt(0)
	v_fmac_f32_e32 v29, v53, v38
	v_fmac_f32_e32 v31, v52, v38
	v_pk_fma_f32 v[0:1], v[6:7], v[28:29], v[0:1] op_sel_hi:[1,0,1]
	v_fmac_f32_e32 v33, v51, v38
	v_pk_fma_f32 v[0:1], v[8:9], v[30:31], v[0:1] op_sel_hi:[1,0,1]
	v_fmac_f32_e32 v35, v50, v38
	v_pk_fma_f32 v[0:1], v[10:11], v[32:33], v[0:1] op_sel_hi:[1,0,1]
	v_fmac_f32_e32 v37, v49, v38
	ds_read_b128 v[48:51], v25 offset:27648
	ds_read_b128 v[52:55], v25 offset:60416
	v_pk_fma_f32 v[0:1], v[12:13], v[34:35], v[0:1] op_sel_hi:[1,0,1]
	v_fmac_f32_e32 v40, v56, v56
	v_pk_fma_f32 v[0:1], v[42:43], v[36:37], v[0:1] op_sel_hi:[1,0,1]
	s_waitcnt lgkmcnt(1)
	v_fmac_f32_e32 v37, v51, v56
	v_pk_fma_f32 v[0:1], v[44:45], v[14:15], v[0:1] op_sel_hi:[1,0,1]
	s_waitcnt lgkmcnt(0)
	v_fmac_f32_e32 v35, v52, v56
	v_pk_fma_f32 v[0:1], v[46:47], v[38:39], v[0:1] op_sel_hi:[1,0,1]
	v_fmac_f32_e32 v39, v50, v56
	v_pk_fma_f32 v[22:23], v[48:49], v[56:57], v[0:1] op_sel_hi:[1,0,1]
	v_fmac_f32_e32 v33, v53, v56
	v_fmac_f32_e32 v31, v54, v56
	v_fmac_f32_e32 v29, v55, v56
	s_waitcnt vmcnt(3)
	v_mov_b32_e32 v0, v68
	v_mov_b32_e32 v1, v69
	v_lshlrev_b32_e32 v24, 16, v0
	v_and_b32_e32 v26, 0xffff0000, v0
	v_lshlrev_b32_e32 v28, 16, v1
	v_and_b32_e32 v30, 0xffff0000, v1
	ds_read_b128 v[0:3], v25 offset:4096
	ds_read_b128 v[4:7], v25 offset:36864
	v_fmac_f32_e32 v40, v24, v24
	v_fmac_f32_e32 v40, v26, v26
	v_fmac_f32_e32 v40, v28, v28
	s_waitcnt lgkmcnt(1)
	v_fmac_f32_e32 v39, v2, v24
	v_fmac_f32_e32 v37, v3, v24
	s_waitcnt lgkmcnt(0)
	v_fmac_f32_e32 v35, v4, v24
	v_fmac_f32_e32 v33, v5, v24
	v_fmac_f32_e32 v31, v6, v24
	v_fmac_f32_e32 v29, v7, v24
	ds_read_b128 v[2:5], v25 offset:12288
	ds_read_b128 v[6:9], v25 offset:45056
	v_pk_fma_f32 v[0:1], v[0:1], v[24:25], v[22:23] op_sel_hi:[1,0,1]
	v_fmac_f32_e32 v40, v30, v30
	s_waitcnt lgkmcnt(1)
	v_fmac_f32_e32 v39, v4, v26
	v_fmac_f32_e32 v37, v5, v26
	s_waitcnt lgkmcnt(0)
	v_fmac_f32_e32 v35, v6, v26
	v_fmac_f32_e32 v33, v7, v26
	v_fmac_f32_e32 v31, v8, v26
	v_fmac_f32_e32 v29, v9, v26
	ds_read_b128 v[4:7], v25 offset:20480
	ds_read_b128 v[8:11], v25 offset:53248
	v_pk_fma_f32 v[0:1], v[2:3], v[26:27], v[0:1] op_sel_hi:[1,0,1]
	s_waitcnt lgkmcnt(1)
	v_fmac_f32_e32 v39, v6, v28
	v_fmac_f32_e32 v37, v7, v28
	s_waitcnt lgkmcnt(0)
	v_fmac_f32_e32 v35, v8, v28
	v_fmac_f32_e32 v33, v9, v28
	v_fmac_f32_e32 v31, v10, v28
	v_fmac_f32_e32 v29, v11, v28
	ds_read_b128 v[6:9], v25 offset:28672
	ds_read_b128 v[10:13], v25 offset:61440
	s_waitcnt lgkmcnt(1)
	v_fmac_f32_e32 v39, v8, v30
	v_fmac_f32_e32 v37, v9, v30
	s_waitcnt lgkmcnt(0)
	v_fmac_f32_e32 v35, v10, v30
	v_fmac_f32_e32 v33, v11, v30
	v_fmac_f32_e32 v31, v12, v30
	v_fmac_f32_e32 v29, v13, v30
	s_waitcnt vmcnt(2)
	v_mov_b32_e32 v8, v70
	v_mov_b32_e32 v9, v71
	v_lshlrev_b32_e32 v32, 16, v8
	v_and_b32_e32 v34, 0xffff0000, v8
	v_lshlrev_b32_e32 v36, 16, v9
	v_and_b32_e32 v38, 0xffff0000, v9
	ds_read_b128 v[8:11], v25 offset:5120
	ds_read_b128 v[12:15], v25 offset:37888
	v_fmac_f32_e32 v40, v32, v32
	v_fmac_f32_e32 v40, v34, v34
	v_fmac_f32_e32 v40, v36, v36
	s_waitcnt lgkmcnt(1)
	v_fmac_f32_e32 v39, v10, v32
	v_fmac_f32_e32 v37, v11, v32
	s_waitcnt lgkmcnt(0)
	v_fmac_f32_e32 v35, v12, v32
	v_fmac_f32_e32 v33, v13, v32
	v_fmac_f32_e32 v31, v14, v32
	v_fmac_f32_e32 v29, v15, v32
	ds_read_b128 v[10:13], v25 offset:13312
	ds_read_b128 v[14:17], v25 offset:46080
	v_fmac_f32_e32 v40, v38, v38
	s_waitcnt lgkmcnt(1)
	v_fmac_f32_e32 v39, v12, v34
	v_fmac_f32_e32 v37, v13, v34
	s_waitcnt lgkmcnt(0)
	v_fmac_f32_e32 v35, v14, v34
	v_fmac_f32_e32 v33, v15, v34
	ds_read_b128 v[12:15], v25 offset:21504
	ds_read_b128 v[42:45], v25 offset:54272
	v_fmac_f32_e32 v31, v16, v34
	v_fmac_f32_e32 v29, v17, v34
	s_waitcnt lgkmcnt(1)
	v_fmac_f32_e32 v39, v14, v36
	v_fmac_f32_e32 v37, v15, v36
	s_waitcnt lgkmcnt(0)
	v_fmac_f32_e32 v35, v42, v36
	v_fmac_f32_e32 v33, v43, v36
	v_fmac_f32_e32 v31, v44, v36
	v_fmac_f32_e32 v29, v45, v36
	ds_read_b128 v[14:17], v25 offset:29696
	ds_read_b128 v[42:45], v25 offset:62464
	s_waitcnt lgkmcnt(1)
	v_fmac_f32_e32 v39, v16, v38
	v_fmac_f32_e32 v37, v17, v38
	s_waitcnt lgkmcnt(0)
	v_fmac_f32_e32 v35, v42, v38
	v_fmac_f32_e32 v33, v43, v38
	v_fmac_f32_e32 v31, v44, v38
	v_fmac_f32_e32 v29, v45, v38
	ds_read_b128 v[42:45], v25 offset:6144
	ds_read_b128 v[46:49], v25 offset:38912
	s_waitcnt vmcnt(1)
	v_mov_b32_e32 v16, v72
	v_mov_b32_e32 v17, v73
	v_lshlrev_b32_e32 v54, 16, v16
	s_waitcnt lgkmcnt(1)
	v_fmac_f32_e32 v39, v44, v54
	v_fmac_f32_e32 v37, v45, v54
	s_waitcnt lgkmcnt(0)
	v_fmac_f32_e32 v35, v46, v54
	v_fmac_f32_e32 v33, v47, v54
	v_fmac_f32_e32 v31, v48, v54
	v_fmac_f32_e32 v29, v49, v54
	ds_read_b128 v[44:47], v25 offset:14336
	ds_read_b128 v[48:51], v25 offset:47104
	v_and_b32_e32 v56, 0xffff0000, v16
	v_lshlrev_b32_e32 v58, 16, v17
	v_and_b32_e32 v16, 0xffff0000, v17
	s_waitcnt lgkmcnt(1)
	v_fmac_f32_e32 v37, v47, v56
	s_waitcnt lgkmcnt(0)
	v_fmac_f32_e32 v29, v51, v56
	v_fmac_f32_e32 v31, v50, v56
	v_pk_fma_f32 v[0:1], v[4:5], v[28:29], v[0:1] op_sel_hi:[1,0,1]
	v_fmac_f32_e32 v33, v49, v56
	v_pk_fma_f32 v[0:1], v[6:7], v[30:31], v[0:1] op_sel_hi:[1,0,1]
	v_fmac_f32_e32 v35, v48, v56
	v_pk_fma_f32 v[0:1], v[8:9], v[32:33], v[0:1] op_sel_hi:[1,0,1]
	v_fmac_f32_e32 v39, v46, v56
	v_pk_fma_f32 v[0:1], v[10:11], v[34:35], v[0:1] op_sel_hi:[1,0,1]
	ds_read_b128 v[46:49], v25 offset:22528
	ds_read_b128 v[50:53], v25 offset:55296
	v_pk_fma_f32 v[0:1], v[12:13], v[36:37], v[0:1] op_sel_hi:[1,0,1]
	v_fmac_f32_e32 v40, v54, v54
	v_pk_fma_f32 v[0:1], v[14:15], v[38:39], v[0:1] op_sel_hi:[1,0,1]
	s_waitcnt lgkmcnt(1)
	v_fmac_f32_e32 v39, v48, v58
	v_pk_fma_f32 v[0:1], v[42:43], v[54:55], v[0:1] op_sel_hi:[1,0,1]
	v_fmac_f32_e32 v37, v49, v58
	v_pk_fma_f32 v[0:1], v[44:45], v[56:57], v[0:1] op_sel_hi:[1,0,1]
	s_waitcnt lgkmcnt(0)
	v_fmac_f32_e32 v35, v50, v58
	v_pk_fma_f32 v[12:13], v[46:47], v[58:59], v[0:1] op_sel_hi:[1,0,1]
	ds_read_b128 v[0:3], v25 offset:30720
	ds_read_b128 v[4:7], v25 offset:63488
	v_fmac_f32_e32 v33, v51, v58
	v_fmac_f32_e32 v31, v52, v58
	v_fmac_f32_e32 v29, v53, v58
	s_waitcnt lgkmcnt(1)
	v_fmac_f32_e32 v39, v2, v16
	v_fmac_f32_e32 v37, v3, v16
	s_waitcnt lgkmcnt(0)
	v_fmac_f32_e32 v35, v4, v16
	v_fmac_f32_e32 v33, v5, v16
	v_fmac_f32_e32 v31, v6, v16
	v_fmac_f32_e32 v29, v7, v16
	v_fmac_f32_e32 v40, v56, v56
	v_fmac_f32_e32 v40, v58, v58
	v_fmac_f32_e32 v40, v16, v16
	s_waitcnt vmcnt(0)
	v_mov_b32_e32 v2, v74
	v_mov_b32_e32 v3, v75
	v_lshlrev_b32_e32 v24, 16, v2
	v_and_b32_e32 v22, 0xffff0000, v2
	v_lshlrev_b32_e32 v20, 16, v3
	v_and_b32_e32 v14, 0xffff0000, v3
	ds_read_b128 v[2:5], v25 offset:7168
	ds_read_b128 v[6:9], v25 offset:39936
	v_fmac_f32_e32 v40, v24, v24
	v_fmac_f32_e32 v40, v22, v22
	v_fmac_f32_e32 v40, v20, v20
	s_waitcnt lgkmcnt(1)
	v_fmac_f32_e32 v39, v4, v24
	v_fmac_f32_e32 v37, v5, v24
	s_waitcnt lgkmcnt(0)
	v_fmac_f32_e32 v35, v6, v24
	v_fmac_f32_e32 v33, v7, v24
	v_fmac_f32_e32 v31, v8, v24
	v_fmac_f32_e32 v29, v9, v24
	ds_read_b128 v[4:7], v25 offset:15360
	ds_read_b128 v[8:11], v25 offset:48128
	v_fmac_f32_e32 v40, v14, v14
	s_waitcnt lgkmcnt(1)
	v_fmac_f32_e32 v39, v6, v22
	v_fmac_f32_e32 v37, v7, v22
	s_waitcnt lgkmcnt(0)
	v_fmac_f32_e32 v35, v8, v22
	v_fmac_f32_e32 v33, v9, v22
	ds_read_b128 v[6:9], v25 offset:23552
	ds_read_b128 v[42:45], v25 offset:56320
	v_fmac_f32_e32 v31, v10, v22
	v_fmac_f32_e32 v29, v11, v22
	s_waitcnt lgkmcnt(1)
	v_fmac_f32_e32 v39, v8, v20
	v_fmac_f32_e32 v37, v9, v20
	s_waitcnt lgkmcnt(0)
	v_fmac_f32_e32 v35, v42, v20
	v_fmac_f32_e32 v33, v43, v20
	v_fmac_f32_e32 v31, v44, v20
	v_fmac_f32_e32 v29, v45, v20
	ds_read_b128 v[8:11], v25 offset:31744
	ds_read_b128 v[42:45], v25 offset:64512
	s_waitcnt lgkmcnt(1)
	v_fmac_f32_e32 v39, v10, v14
	v_mbcnt_lo_u32_b32 v10, -1, 0
	v_mbcnt_hi_u32_b32 v10, -1, v10
	v_fmac_f32_e32 v37, v11, v14
	v_lshlrev_b32_e32 v10, 2, v10
	v_xor_b32_e32 v10, 4, v10
	ds_bpermute_b32 v10, v10, v40
	v_mbcnt_lo_u32_b32 v11, -1, 0
	v_mbcnt_hi_u32_b32 v11, -1, v11
	s_waitcnt lgkmcnt(1)
	v_fmac_f32_e32 v35, v42, v14
	v_lshlrev_b32_e32 v11, 2, v11
	v_xor_b32_e32 v11, 8, v11
	s_waitcnt lgkmcnt(0)
	v_add_f32_e32 v10, v40, v10
	ds_bpermute_b32 v11, v11, v10
	v_fmac_f32_e32 v33, v43, v14
	v_fmac_f32_e32 v31, v44, v14
	v_fmac_f32_e32 v29, v45, v14
	s_waitcnt lgkmcnt(0)
	v_add_f32_e32 v10, v10, v11
	v_mbcnt_lo_u32_b32 v11, -1, 0
	v_mbcnt_hi_u32_b32 v11, -1, v11
	s_nop 0
	v_lshlrev_b32_e32 v11, 2, v11
	v_xor_b32_e32 v11, 16, v11
	ds_bpermute_b32 v11, v11, v10
	s_waitcnt lgkmcnt(0)
	v_add_f32_e32 v10, v10, v11
	v_mbcnt_lo_u32_b32 v11, -1, 0
	v_mbcnt_hi_u32_b32 v11, -1, v11
	s_nop 0
	v_lshlrev_b32_e32 v11, 2, v11
	v_xor_b32_e32 v11, 32, v11
	ds_bpermute_b32 v11, v11, v10
	s_waitcnt lgkmcnt(0)
	v_add_f32_e32 v10, v10, v11
	v_mbcnt_lo_u32_b32 v11, -1, 0
	v_mbcnt_hi_u32_b32 v11, -1, v11
	s_nop 0
	v_lshlrev_b32_e32 v11, 2, v11
	v_xor_b32_e32 v11, 64, v11
	ds_bpermute_b32 v11, v11, v10
	s_waitcnt lgkmcnt(0)
	v_add_f32_e32 v10, v10, v11
	v_mbcnt_lo_u32_b32 v11, -1, 0
	v_mbcnt_hi_u32_b32 v11, -1, v11
	v_mbcnt_lo_u32_b32 v15, -1, 0
	v_mbcnt_hi_u32_b32 v15, -1, v15
	v_mbcnt_lo_u32_b32 v17, -1, 0
	v_mbcnt_hi_u32_b32 v17, -1, v17
	v_mbcnt_lo_u32_b32 v21, -1, 0
	v_mbcnt_hi_u32_b32 v21, -1, v21
	v_mbcnt_lo_u32_b32 v23, -1, 0
	v_mbcnt_hi_u32_b32 v23, -1, v23
	v_mbcnt_lo_u32_b32 v26, -1, 0
	v_mbcnt_hi_u32_b32 v26, -1, v26
	v_mbcnt_lo_u32_b32 v27, -1, 0
	v_mbcnt_hi_u32_b32 v27, -1, v27
	s_nop 0
	v_lshlrev_b32_e32 v15, 2, v15
	v_lshlrev_b32_e32 v17, 2, v17
	v_xor_b32_e32 v17, 8, v17
	v_lshlrev_b32_e32 v23, 2, v23
	v_pk_fma_f32 v[0:1], v[0:1], v[16:17], v[12:13] op_sel_hi:[1,0,1]
	v_lshlrev_b32_e32 v21, 2, v21
	v_xor_b32_e32 v23, 32, v23
	v_pk_fma_f32 v[0:1], v[2:3], v[24:25], v[0:1] op_sel_hi:[1,0,1]
	v_xor_b32_e32 v21, 16, v21
	v_mbcnt_lo_u32_b32 v28, -1, 0
	v_mbcnt_hi_u32_b32 v28, -1, v28
	v_pk_fma_f32 v[0:1], v[4:5], v[22:23], v[0:1] op_sel_hi:[1,0,1]
	v_xor_b32_e32 v15, 4, v15
	v_lshlrev_b32_e32 v28, 2, v28
	v_pk_fma_f32 v[0:1], v[6:7], v[20:21], v[0:1] op_sel_hi:[1,0,1]
	v_xor_b32_e32 v28, 4, v28
	v_pk_fma_f32 v[0:1], v[8:9], v[14:15], v[0:1] op_sel_hi:[1,0,1]
	v_mbcnt_lo_u32_b32 v41, -1, 0
	v_mbcnt_hi_u32_b32 v41, -1, v41
	v_lshlrev_b32_e32 v41, 2, v41
	v_xor_b32_e32 v42, 4, v41
	ds_bpermute_b32 v2, v42, v0
	ds_bpermute_b32 v3, v42, v1
	ds_bpermute_b32 v43, v42, v39
	ds_bpermute_b32 v44, v42, v37
	ds_bpermute_b32 v45, v42, v35
	ds_bpermute_b32 v46, v42, v33
	ds_bpermute_b32 v47, v42, v31
	ds_bpermute_b32 v48, v42, v29
	s_waitcnt lgkmcnt(0)
	v_pk_add_f32 v[0:1], v[0:1], v[2:3]
	v_add_f32_e32 v39, v39, v43
	v_add_f32_e32 v37, v37, v44
	v_add_f32_e32 v35, v35, v45
	v_add_f32_e32 v33, v33, v46
	v_add_f32_e32 v31, v31, v47
	v_add_f32_e32 v29, v29, v48
	v_xor_b32_e32 v42, 8, v41
	ds_bpermute_b32 v2, v42, v0
	ds_bpermute_b32 v3, v42, v1
	ds_bpermute_b32 v43, v42, v39
	ds_bpermute_b32 v44, v42, v37
	ds_bpermute_b32 v45, v42, v35
	ds_bpermute_b32 v46, v42, v33
	ds_bpermute_b32 v47, v42, v31
	ds_bpermute_b32 v48, v42, v29
	s_waitcnt lgkmcnt(0)
	v_pk_add_f32 v[0:1], v[0:1], v[2:3]
	v_add_f32_e32 v39, v39, v43
	v_add_f32_e32 v37, v37, v44
	v_add_f32_e32 v35, v35, v45
	v_add_f32_e32 v33, v33, v46
	v_add_f32_e32 v31, v31, v47
	v_add_f32_e32 v29, v29, v48
	v_xor_b32_e32 v42, 16, v41
	ds_bpermute_b32 v2, v42, v0
	ds_bpermute_b32 v3, v42, v1
	ds_bpermute_b32 v43, v42, v39
	ds_bpermute_b32 v44, v42, v37
	ds_bpermute_b32 v45, v42, v35
	ds_bpermute_b32 v46, v42, v33
	ds_bpermute_b32 v47, v42, v31
	ds_bpermute_b32 v48, v42, v29
	s_waitcnt lgkmcnt(0)
	v_pk_add_f32 v[0:1], v[0:1], v[2:3]
	v_add_f32_e32 v39, v39, v43
	v_add_f32_e32 v37, v37, v44
	v_add_f32_e32 v35, v35, v45
	v_add_f32_e32 v33, v33, v46
	v_add_f32_e32 v31, v31, v47
	v_add_f32_e32 v29, v29, v48
	v_xor_b32_e32 v42, 32, v41
	ds_bpermute_b32 v2, v42, v0
	ds_bpermute_b32 v3, v42, v1
	ds_bpermute_b32 v43, v42, v39
	ds_bpermute_b32 v44, v42, v37
	ds_bpermute_b32 v45, v42, v35
	ds_bpermute_b32 v46, v42, v33
	ds_bpermute_b32 v47, v42, v31
	ds_bpermute_b32 v48, v42, v29
	s_waitcnt lgkmcnt(0)
	v_pk_add_f32 v[0:1], v[0:1], v[2:3]
	v_add_f32_e32 v39, v39, v43
	v_add_f32_e32 v37, v37, v44
	v_add_f32_e32 v35, v35, v45
	v_add_f32_e32 v33, v33, v46
	v_add_f32_e32 v31, v31, v47
	v_add_f32_e32 v29, v29, v48
	v_xor_b32_e32 v42, 64, v41
	ds_bpermute_b32 v2, v42, v0
	ds_bpermute_b32 v3, v42, v1
	ds_bpermute_b32 v43, v42, v39
	ds_bpermute_b32 v44, v42, v37
	ds_bpermute_b32 v45, v42, v35
	ds_bpermute_b32 v46, v42, v33
	ds_bpermute_b32 v47, v42, v31
	ds_bpermute_b32 v48, v42, v29
	s_waitcnt lgkmcnt(0)
	v_pk_add_f32 v[0:1], v[0:1], v[2:3]
	v_add_f32_e32 v39, v39, v43
	v_add_f32_e32 v37, v37, v44
	v_add_f32_e32 v35, v35, v45
	v_add_f32_e32 v33, v33, v46
	v_add_f32_e32 v31, v31, v47
	v_add_f32_e32 v29, v29, v48
	v_xor_b32_e32 v42, 0x80, v41
	ds_bpermute_b32 v2, v42, v0
	ds_bpermute_b32 v3, v42, v1
	ds_bpermute_b32 v11, v42, v10
	ds_bpermute_b32 v6, v42, v39
	ds_bpermute_b32 v8, v42, v37
	ds_bpermute_b32 v12, v42, v35
	ds_bpermute_b32 v14, v42, v33
	ds_bpermute_b32 v16, v42, v31
	ds_bpermute_b32 v20, v42, v29
	v_mov_b32_e32 v5, v39
	v_mov_b32_e32 v7, v37
	v_mov_b32_e32 v9, v35
	v_mov_b32_e32 v13, v33
	v_mov_b32_e32 v15, v31
	v_mov_b32_e32 v17, v29
	s_waitcnt lgkmcnt(0)
	s_and_saveexec_b64 s[0:1], s[36:37]
	s_cbranch_execz .LBB0_1621
	v_add_f32_e32 v4, v10, v11
	v_fmamk_f32 v4, v4, 0x3a000000, v253
	s_mov_b32 s13, 0xf800000
	v_cmp_gt_f32_e32 vcc, s13, v4
	v_mul_f32_e32 v10, 0x4f800000, v4
	v_add_f32_e32 v5, v5, v6
	v_cndmask_b32_e32 v4, v4, v10, vcc
	v_sqrt_f32_e32 v10, v4
	v_pk_add_f32 v[0:1], v[0:1], v[2:3]
	v_add_f32_e32 v7, v7, v8
	v_add_f32_e32 v9, v9, v12
	v_add_u32_e32 v11, -1, v10
	v_fma_f32 v21, -v11, v10, v4
	v_cmp_ge_f32_e64 s[38:39], 0, v21
	v_add_u32_e32 v21, 1, v10
	v_add_f32_e32 v13, v13, v14
	v_cndmask_b32_e64 v11, v10, v11, s[38:39]
	v_fma_f32 v10, -v21, v10, v4
	v_cmp_lt_f32_e64 s[38:39], 0, v10
	s_nop 1
	v_cndmask_b32_e64 v10, v11, v21, s[38:39]
	v_mul_f32_e32 v11, 0x37800000, v10
	v_cndmask_b32_e32 v10, v10, v11, vcc
	v_mov_b32_e32 v11, 0x260
	v_cmp_class_f32_e32 vcc, v4, v11
	s_nop 1
	v_cndmask_b32_e32 v4, v10, v4, vcc
	v_div_scale_f32 v10, s[18:19], v4, v4, 1.0
	v_rcp_f32_e32 v11, v10
	s_nop 0
	v_fma_f32 v21, -v10, v11, 1.0
	v_fmac_f32_e32 v11, v21, v11
	v_div_scale_f32 v21, vcc, 1.0, v4, 1.0
	v_mul_f32_e32 v22, v21, v11
	v_fma_f32 v23, -v10, v22, v21
	v_fmac_f32_e32 v22, v23, v11
	v_fma_f32 v10, -v10, v22, v21
	v_div_fmas_f32 v10, v10, v11, v22
	v_div_fixup_f32 v4, v10, v4, 1.0
	v_mul_f32_e32 v5, v4, v5
	v_pk_mul_f32 v[0:1], v[4:5], v[0:1] op_sel_hi:[0,1]
	v_cmp_gt_f32_e32 vcc, v1, v0
	v_mul_f32_e32 v7, v4, v7
	v_mul_f32_e32 v9, v4, v9
	v_cndmask_b32_e32 v2, v0, v1, vcc
	v_cmp_gt_f32_e64 s[38:39], v5, v2
	v_mul_f32_e32 v13, v4, v13
	v_cndmask_b32_e64 v3, 0, 1, vcc
	v_cndmask_b32_e64 v2, v2, v5, s[38:39]
	v_cmp_gt_f32_e64 s[40:41], v7, v2
	v_add_f32_e32 v11, v15, v16
	v_cndmask_b32_e64 v3, v3, 2, s[38:39]
	v_cndmask_b32_e64 v2, v2, v7, s[40:41]
	v_cmp_gt_f32_e64 s[42:43], v9, v2
	v_mul_f32_e32 v11, v4, v11
	v_cndmask_b32_e64 v3, v3, 3, s[40:41]
	v_cndmask_b32_e64 v2, v2, v9, s[42:43]
	v_cmp_gt_f32_e64 s[44:45], v13, v2
	s_waitcnt lgkmcnt(0)
	v_add_f32_e32 v10, v17, v20
	v_cndmask_b32_e64 v3, v3, 4, s[42:43]
	v_cndmask_b32_e64 v2, v2, v13, s[44:45]
	v_cmp_gt_f32_e64 s[46:47], v11, v2
	v_mul_f32_e32 v10, v4, v10
	v_cndmask_b32_e64 v3, v3, 5, s[44:45]
	v_cndmask_b32_e64 v2, v2, v11, s[46:47]
	v_cmp_ngt_f32_e64 s[48:49], v10, v2
	v_cndmask_b32_e64 v3, v3, 6, s[46:47]
	s_and_b64 s[18:19], s[48:49], s[46:47]
	v_cndmask_b32_e64 v176, 7, v3, s[48:49]
	v_cmp_ne_u32_e64 s[46:47], 0, v176
	v_cmp_lt_f32_e64 s[50:51], s11, v0
	s_and_b64 s[46:47], s[46:47], s[50:51]
	v_mov_b32_e32 v3, 0xff61b1e6
	v_cndmask_b32_e64 v0, v3, v0, s[46:47]
	v_cmp_ne_u32_e64 s[44:45], 1, v176
	v_cmp_gt_f32_e64 s[46:47], v1, v0
	s_and_b64 s[44:45], s[44:45], s[46:47]
	v_cndmask_b32_e64 v0, v0, v1, s[44:45]
	v_cmp_ne_u32_e64 s[42:43], 2, v176
	v_cmp_gt_f32_e64 s[46:47], v5, v0
	s_and_b64 s[42:43], s[42:43], s[46:47]
	v_cndmask_b32_e64 v0, v0, v5, s[42:43]
	v_cmp_ne_u32_e64 s[40:41], 3, v176
	v_cmp_gt_f32_e64 s[46:47], v7, v0
	s_and_b64 s[40:41], s[40:41], s[46:47]
	v_cndmask_b32_e64 v0, v0, v7, s[40:41]
	v_cmp_ne_u32_e64 s[38:39], 4, v176
	v_cmp_gt_f32_e64 s[46:47], v9, v0
	s_and_b64 s[38:39], s[38:39], s[46:47]
	v_cndmask_b32_e64 v0, v0, v9, s[38:39]
	v_cmp_ne_u32_e32 vcc, 5, v176
	v_cmp_gt_f32_e64 s[46:47], v13, v0
	s_and_b64 vcc, vcc, s[46:47]
	v_cndmask_b32_e32 v0, v0, v13, vcc
	v_cmp_ngt_f32_e64 s[46:47], v11, v0
	s_or_b64 s[46:47], s[18:19], s[46:47]
	v_cndmask_b32_e64 v2, v10, v2, s[48:49]
	v_cndmask_b32_e64 v1, v11, v0, s[46:47]
	v_cmp_gt_f32_e64 s[50:51], v10, v1
	s_and_b64 s[50:51], s[48:49], s[50:51]
	v_cndmask_b32_e64 v0, 0, 1, s[44:45]
	v_cndmask_b32_e64 v1, v1, v10, s[50:51]
	v_sub_f32_e32 v1, v2, v1
	v_mul_f32_e32 v1, 0x3fb8aa3b, v1
	v_exp_f32_e32 v1, v1
	v_cndmask_b32_e64 v0, v0, 2, s[42:43]
	v_cndmask_b32_e64 v0, v0, 3, s[40:41]
	v_cndmask_b32_e64 v0, v0, 4, s[38:39]
	v_add_f32_e32 v1, 1.0, v1
	v_div_scale_f32 v2, s[18:19], v1, v1, 1.0
	v_rcp_f32_e32 v3, v2
	v_cndmask_b32_e64 v0, v0, 5, vcc
	s_add_u32 s18, s52, s8
	s_addc_u32 s19, s53, s9
	v_fma_f32 v5, -v2, v3, 1.0
	v_fmac_f32_e32 v3, v5, v3
	v_div_scale_f32 v5, vcc, 1.0, v1, 1.0
	v_mul_f32_e32 v6, v5, v3
	v_fma_f32 v7, -v2, v6, v5
	v_fmac_f32_e32 v6, v7, v3
	v_fma_f32 v2, -v2, v6, v5
	v_div_fmas_f32 v2, v2, v3, v6
	v_div_fixup_f32 v5, v2, v1, 1.0
	v_cndmask_b32_e64 v0, 6, v0, s[46:47]
	v_cndmask_b32_e64 v0, v0, 7, s[50:51]
	v_sub_f32_e32 v10, 1.0, v5
	v_mov_b32_e32 v80, v176
	v_mov_b32_e32 v81, v0
	v_mov_b32_e32 v82, v4
	v_mov_b32_e32 v83, v10
	v_mov_b32_e32 v84, v5
	v_mov_b32_e32 v85, s56
	v_mov_b32_e32 v6, s99
	ds_write_b128 v6, v[80:83]
	ds_write_b64 v6, v[84:85] offset:16
	s_add_i32 s99, s99, 32
	s_branch .LBB0_1621
.LBB0_1624:
	s_waitcnt lgkmcnt(0)
	s_barrier
	s_cmp_lg_u32 s91, 0
	s_cbranch_scc1 .Lrt_done
	v_mbcnt_lo_u32_b32 v6, -1, 0
	v_mbcnt_hi_u32_b32 v6, -1, v6
	v_lshlrev_b32_e32 v7, 5, v6
	v_add_u32_e32 v7, 0x10000, v7
	ds_read_b128 v[80:83], v7
	ds_read_b64 v[84:85], v7 offset:16
	v_mov_b32_e32 v86, 0
	v_mov_b32_e32 v87, 0
	v_mov_b32_e32 v88, 0
	s_waitcnt lgkmcnt(0)
	v_cmp_eq_u32_e64 s[38:39], 0, v80
	v_cmp_eq_u32_e64 s[40:41], 0, v81
	s_nop 1
	s_bcnt1_i32_b64 s42, s[38:39]
	s_bcnt1_i32_b64 s43, s[40:41]
	v_mbcnt_lo_u32_b32 v89, s38, 0
	v_mbcnt_hi_u32_b32 v89, s39, v89
	v_mbcnt_lo_u32_b32 v90, s40, 0
	v_mbcnt_hi_u32_b32 v90, s41, v90
	v_add_u32_e32 v90, s42, v90
	v_cndmask_b32_e64 v86, v86, v89, s[38:39]
	v_cndmask_b32_e64 v87, v87, v90, s[40:41]
	s_add_i32 s42, s42, s43
	v_writelane_b32 v88, s42, 0
	v_cmp_eq_u32_e64 s[38:39], 1, v80
	v_cmp_eq_u32_e64 s[40:41], 1, v81
	s_nop 1
	s_bcnt1_i32_b64 s42, s[38:39]
	s_bcnt1_i32_b64 s43, s[40:41]
	v_mbcnt_lo_u32_b32 v89, s38, 0
	v_mbcnt_hi_u32_b32 v89, s39, v89
	v_mbcnt_lo_u32_b32 v90, s40, 0
	v_mbcnt_hi_u32_b32 v90, s41, v90
	v_add_u32_e32 v90, s42, v90
	v_cndmask_b32_e64 v86, v86, v89, s[38:39]
	v_cndmask_b32_e64 v87, v87, v90, s[40:41]
	s_add_i32 s42, s42, s43
	v_writelane_b32 v88, s42, 1
	v_cmp_eq_u32_e64 s[38:39], 2, v80
	v_cmp_eq_u32_e64 s[40:41], 2, v81
	s_nop 1
	s_bcnt1_i32_b64 s42, s[38:39]
	s_bcnt1_i32_b64 s43, s[40:41]
	v_mbcnt_lo_u32_b32 v89, s38, 0
	v_mbcnt_hi_u32_b32 v89, s39, v89
	v_mbcnt_lo_u32_b32 v90, s40, 0
	v_mbcnt_hi_u32_b32 v90, s41, v90
	v_add_u32_e32 v90, s42, v90
	v_cndmask_b32_e64 v86, v86, v89, s[38:39]
	v_cndmask_b32_e64 v87, v87, v90, s[40:41]
	s_add_i32 s42, s42, s43
	v_writelane_b32 v88, s42, 2
	v_cmp_eq_u32_e64 s[38:39], 3, v80
	v_cmp_eq_u32_e64 s[40:41], 3, v81
	s_nop 1
	s_bcnt1_i32_b64 s42, s[38:39]
	s_bcnt1_i32_b64 s43, s[40:41]
	v_mbcnt_lo_u32_b32 v89, s38, 0
	v_mbcnt_hi_u32_b32 v89, s39, v89
	v_mbcnt_lo_u32_b32 v90, s40, 0
	v_mbcnt_hi_u32_b32 v90, s41, v90
	v_add_u32_e32 v90, s42, v90
	v_cndmask_b32_e64 v86, v86, v89, s[38:39]
	v_cndmask_b32_e64 v87, v87, v90, s[40:41]
	s_add_i32 s42, s42, s43
	v_writelane_b32 v88, s42, 3
	v_cmp_eq_u32_e64 s[38:39], 4, v80
	v_cmp_eq_u32_e64 s[40:41], 4, v81
	s_nop 1
	s_bcnt1_i32_b64 s42, s[38:39]
	s_bcnt1_i32_b64 s43, s[40:41]
	v_mbcnt_lo_u32_b32 v89, s38, 0
	v_mbcnt_hi_u32_b32 v89, s39, v89
	v_mbcnt_lo_u32_b32 v90, s40, 0
	v_mbcnt_hi_u32_b32 v90, s41, v90
	v_add_u32_e32 v90, s42, v90
	v_cndmask_b32_e64 v86, v86, v89, s[38:39]
	v_cndmask_b32_e64 v87, v87, v90, s[40:41]
	s_add_i32 s42, s42, s43
	v_writelane_b32 v88, s42, 4
	v_cmp_eq_u32_e64 s[38:39], 5, v80
	v_cmp_eq_u32_e64 s[40:41], 5, v81
	s_nop 1
	s_bcnt1_i32_b64 s42, s[38:39]
	s_bcnt1_i32_b64 s43, s[40:41]
	v_mbcnt_lo_u32_b32 v89, s38, 0
	v_mbcnt_hi_u32_b32 v89, s39, v89
	v_mbcnt_lo_u32_b32 v90, s40, 0
	v_mbcnt_hi_u32_b32 v90, s41, v90
	v_add_u32_e32 v90, s42, v90
	v_cndmask_b32_e64 v86, v86, v89, s[38:39]
	v_cndmask_b32_e64 v87, v87, v90, s[40:41]
	s_add_i32 s42, s42, s43
	v_writelane_b32 v88, s42, 5
	v_cmp_eq_u32_e64 s[38:39], 6, v80
	v_cmp_eq_u32_e64 s[40:41], 6, v81
	s_nop 1
	s_bcnt1_i32_b64 s42, s[38:39]
	s_bcnt1_i32_b64 s43, s[40:41]
	v_mbcnt_lo_u32_b32 v89, s38, 0
	v_mbcnt_hi_u32_b32 v89, s39, v89
	v_mbcnt_lo_u32_b32 v90, s40, 0
	v_mbcnt_hi_u32_b32 v90, s41, v90
	v_add_u32_e32 v90, s42, v90
	v_cndmask_b32_e64 v86, v86, v89, s[38:39]
	v_cndmask_b32_e64 v87, v87, v90, s[40:41]
	s_add_i32 s42, s42, s43
	v_writelane_b32 v88, s42, 6
	v_cmp_eq_u32_e64 s[38:39], 7, v80
	v_cmp_eq_u32_e64 s[40:41], 7, v81
	s_nop 1
	s_bcnt1_i32_b64 s42, s[38:39]
	s_bcnt1_i32_b64 s43, s[40:41]
	v_mbcnt_lo_u32_b32 v89, s38, 0
	v_mbcnt_hi_u32_b32 v89, s39, v89
	v_mbcnt_lo_u32_b32 v90, s40, 0
	v_mbcnt_hi_u32_b32 v90, s41, v90
	v_add_u32_e32 v90, s42, v90
	v_cndmask_b32_e64 v86, v86, v89, s[38:39]
	v_cndmask_b32_e64 v87, v87, v90, s[40:41]
	s_add_i32 s42, s42, s43
	v_writelane_b32 v88, s42, 7
	s_mov_b64 exec, 0xff
	v_mul_u32_u24_e32 v91, 0x2100, v6
	global_atomic_add v92, v91, v88, s[52:53] offset:384 sc0
	s_mov_b64 exec, -1
	v_lshlrev_b32_e32 v93, 2, v80
	v_lshlrev_b32_e32 v94, 2, v81
	s_add_u32 s20, s52, 0x300000
	s_addc_u32 s21, s53, 0
	s_add_u32 s22, s52, 0x380000
	s_addc_u32 s23, s53, 0
	s_add_u32 s44, s52, 0x400000
	s_addc_u32 s45, s53, 0
	s_add_u32 s46, s52, 0x420000
	s_addc_u32 s47, s53, 0
	s_add_u32 s48, s52, 0x440000
	s_addc_u32 s49, s53, 0
	s_waitcnt vmcnt(0)
	ds_bpermute_b32 v93, v93, v92
	ds_bpermute_b32 v94, v94, v92
	v_cmp_ne_u32_e32 vcc, 0xff, v80
	s_waitcnt lgkmcnt(0)
	v_add_u32_e32 v93, v93, v86
	v_add_u32_e32 v94, v94, v87
	s_and_saveexec_b64 s[38:39], vcc
	s_cbranch_execz .Lrt_nostore
	v_lshl_add_u32 v100, v80, 14, v93
	v_lshl_add_u32 v101, v81, 14, v94
	v_lshlrev_b32_e32 v97, 2, v100
	v_lshlrev_b32_e32 v98, 2, v101
	v_lshlrev_b32_e32 v95, 2, v85
	v_lshlrev_b32_e32 v96, 3, v85
	v_mov_b32_e32 v102, v83
	v_mov_b32_e32 v103, v84
	global_store_dword v95, v82, s[44:45]
	global_store_dwordx2 v96, v[102:103], s[48:49]
	global_store_dword v97, v85, s[20:21]
	global_store_dword v98, v85, s[20:21]
	global_store_dword v97, v82, s[22:23]
	global_store_dword v98, v82, s[22:23]
	global_store_dwordx2 v96, v[100:101], s[46:47]
.Lrt_nostore:
	s_or_b64 exec, exec, s[38:39]
